# nt hints only where one instruction consumes whole lines: + final phase x loads / output stores, P6 projection stores, phase-0 x and mem row loads
# speedup vs baseline: 1.0178x; 1.0178x over previous
.LBB0_123:
	v_lshl_add_u64 v[16:17], v[6:7], 0, s[20:21]
	s_mov_b64 s[8:9], 0x1f800000
	v_lshl_add_u64 v[20:21], v[16:17], 0, s[8:9]
	v_add_co_u32_e32 v16, vcc, 0x1f800000, v16
	global_load_dwordx4 v[8:11], v[20:21], off offset:16 nt
	global_load_dwordx4 v[12:15], v[20:21], off offset:32 nt
	v_addc_co_u32_e32 v17, vcc, 0, v17, vcc
	global_load_dwordx4 v[16:19], v[16:17], off nt
	s_nop 0
	global_load_dwordx4 v[20:23], v[20:21], off offset:48 nt
	v_add_u32_e32 v2, s92, v2
	v_cmp_lt_i32_e32 vcc, s1, v2
	s_or_b64 s[6:7], vcc, s[6:7]
	v_lshl_add_u64 v[24:25], v[4:5], 0, s[20:21]
	v_lshl_add_u64 v[4:5], v[4:5], 0, s[22:23]
	v_lshl_add_u64 v[6:7], v[6:7], 0, s[12:13]
	s_waitcnt vmcnt(0)
	v_mov_b32_e32 v26, v9
	v_mov_b32_e32 v27, v10
	v_mov_b32_e32 v9, v11
	s_waitcnt vmcnt(2)
	v_add_f32_e32 v10, v12, v13
	v_add_f32_e32 v12, v14, v15
	s_waitcnt vmcnt(1)
	v_mov_b32_e32 v14, v17
	v_mov_b32_e32 v15, v18
	v_mov_b32_e32 v17, v19
	v_pk_add_f32 v[8:9], v[26:27], v[8:9]
	s_waitcnt vmcnt(0)
	v_mov_b32_e32 v11, v22
	v_mov_b32_e32 v13, v23
	v_pk_add_f32 v[14:15], v[14:15], v[16:17]
	v_pk_add_f32 v[8:9], v[8:9], v[8:9] op_sel:[0,1] op_sel_hi:[1,0]
	v_pk_add_f32 v[10:11], v[10:11], v[12:13]
	v_pk_add_f32 v[12:13], v[14:15], v[14:15] op_sel:[0,1] op_sel_hi:[1,0]
	v_mov_b32_e32 v9, v21
	v_mov_b32_e32 v13, v20
	v_pk_add_f32 v[8:9], v[12:13], v[8:9]
	s_nop 0
	v_pk_add_f32 v[8:9], v[8:9], v[10:11]
	s_nop 0
	v_add_f32_e32 v8, v8, v9
	v_fmamk_f32 v8, v8, 0x3a800000, v1
	v_mul_f32_e32 v9, 0x4f800000, v8
	v_cmp_gt_f32_e32 vcc, s29, v8
	s_nop 1
	v_cndmask_b32_e32 v8, v8, v9, vcc
	v_sqrt_f32_e32 v9, v8
	s_nop 0
	v_add_u32_e32 v10, -1, v9
	v_add_u32_e32 v11, 1, v9
	v_fma_f32 v12, -v10, v9, v8
	v_fma_f32 v13, -v11, v9, v8
	v_cmp_ge_f32_e64 s[38:39], 0, v12
	s_nop 1
	v_cndmask_b32_e64 v9, v9, v10, s[38:39]
	v_cmp_lt_f32_e64 s[38:39], 0, v13
	s_nop 1
	v_cndmask_b32_e64 v9, v9, v11, s[38:39]
	v_mul_f32_e32 v10, 0x37800000, v9
	v_cndmask_b32_e32 v9, v9, v10, vcc
	v_cmp_class_f32_e32 vcc, v8, v248
	s_nop 1
	v_cndmask_b32_e32 v8, v9, v8, vcc
	v_div_scale_f32 v9, s[8:9], v8, v8, 1.0
	v_rcp_f32_e32 v10, v9
	v_div_scale_f32 v11, vcc, 1.0, v8, 1.0
	v_fma_f32 v12, -v9, v10, 1.0
	v_fmac_f32_e32 v10, v12, v10
	v_mul_f32_e32 v12, v11, v10
	v_fma_f32 v13, -v9, v12, v11
	v_fmac_f32_e32 v12, v13, v10
	v_fma_f32 v9, -v9, v12, v11
	v_div_fmas_f32 v9, v9, v10, v12
	v_div_fixup_f32 v8, v9, v8, 1.0
	global_store_dword v[24:25], v8, off
	s_andn2_b64 exec, exec, s[6:7]
	s_cbranch_execnz .LBB0_123

.LBB0_129:
	s_add_i32 s13, s90, s12
	s_cmp_lt_i32 s13, 0x8000
	s_cselect_b64 s[4:5], -1, 0
	s_and_b64 s[16:17], s[4:5], exec
	s_cselect_b32 s16, s13, s12
	s_ashr_i32 s17, s16, 31
	s_lshl_b64 s[16:17], s[16:17], 12
	global_load_dwordx4 v[28:31], v[44:45], off offset:-3072 nt
	s_waitcnt lgkmcnt(0)
	v_lshl_add_u64 v[4:5], v[38:39], 0, s[16:17]
	global_load_dwordx4 v[24:27], v[44:45], off offset:-2048 nt
	global_load_dwordx4 v[32:35], v[4:5], off nt
	global_load_dwordx4 v[20:23], v[4:5], off offset:1024 nt
	global_load_dwordx4 v[16:19], v[44:45], off offset:-1024 nt
	global_load_dwordx4 v[8:11], v[44:45], off nt
	global_load_dwordx4 v[12:15], v[4:5], off offset:2048 nt
	s_nop 0
	global_load_dwordx4 v[4:7], v[4:5], off offset:3072 nt
	v_lshl_add_u64 v[48:49], v[42:43], 0, s[20:21]
	v_lshl_add_u64 v[46:47], v[40:41], 0, s[20:21]
	s_cmpk_gt_i32 s13, 0x7fff
	s_waitcnt vmcnt(0)
	v_bfe_u32 v2, v28, 16, 1
	v_bfe_u32 v53, v29, 16, 1
	v_add3_u32 v2, v28, v2, s1
	v_bfe_u32 v54, v30, 16, 1
	v_add3_u32 v53, v29, v53, s1
	v_lshrrev_b32_e32 v2, 16, v2
	v_add3_u32 v55, v30, v54, s1
	v_and_or_b32 v54, v53, s0, v2
	v_bfe_u32 v53, v31, 16, 1
	v_lshrrev_b32_e32 v2, 16, v55
	v_add3_u32 v53, v31, v53, s1
	v_and_or_b32 v55, v53, s0, v2
	global_store_dwordx2 v[48:49], v[54:55], off offset:-1024
	s_cbranch_scc1 .LBB0_131
	s_waitcnt vmcnt(6)
	v_bfe_u32 v2, v32, 16, 1
	v_add3_u32 v2, v32, v2, s1
	v_bfe_u32 v53, v33, 16, 1
	v_lshrrev_b32_e32 v2, 16, v2
	v_add3_u32 v53, v33, v53, s1
	v_and_or_b32 v54, v53, s0, v2
	v_bfe_u32 v2, v34, 16, 1
	v_add3_u32 v2, v34, v2, s1
	v_bfe_u32 v53, v35, 16, 1
	v_lshrrev_b32_e32 v2, 16, v2
	v_add3_u32 v53, v35, v53, s1
	v_and_or_b32 v55, v53, s0, v2
	global_store_dwordx2 v[46:47], v[54:55], off offset:-1024

.LBB0_142:
	global_load_dwordx4 v[16:19], v[10:11], off offset:-2048 nt
	global_load_dwordx4 v[20:23], v[10:11], off offset:-1024 nt
	global_load_dwordx4 v[24:27], v[10:11], off nt
	global_load_dwordx4 v[4:7], v[10:11], off offset:1024 nt
	global_load_dwordx4 v[28:31], v[8:9], off nt
	s_add_i32 s18, s18, s90
	v_lshl_add_u64 v[10:11], v[10:11], 0, s[12:13]
	s_cmpk_gt_i32 s18, 0x7ff
	s_waitcnt vmcnt(0)
	v_mul_f32_e32 v2, v17, v17
	v_mul_f32_e32 v32, v19, v19
	s_waitcnt vmcnt(3)
	v_mul_f32_e32 v33, v21, v21
	v_mul_f32_e32 v34, v23, v23
	s_waitcnt vmcnt(2)
	v_mul_f32_e32 v35, v25, v25
	v_mul_f32_e32 v37, v27, v27
	v_fmac_f32_e32 v2, v16, v16
	v_fmac_f32_e32 v32, v18, v18
	v_fmac_f32_e32 v33, v20, v20
	v_fmac_f32_e32 v34, v22, v22
	s_waitcnt vmcnt(1)
	v_mul_f32_e32 v38, v5, v5
	v_mul_f32_e32 v39, v7, v7
	v_fmac_f32_e32 v35, v24, v24
	v_fmac_f32_e32 v37, v26, v26
	v_add_f32_e32 v2, v2, v32
	v_add_f32_e32 v32, v33, v34
	v_fmac_f32_e32 v38, v4, v4
	v_fmac_f32_e32 v39, v6, v6
	v_add_f32_e32 v33, v35, v37
	v_add_f32_e32 v2, v2, v32
	v_add_f32_e32 v34, v38, v39
	v_add_f32_e32 v2, v2, v33
	v_add_f32_e32 v2, v2, v34
	s_nop 1
	v_add_f32_dpp v2, v2, v2 quad_perm:[1,0,3,2] row_mask:0xf bank_mask:0xf bound_ctrl:1
	s_nop 1
	v_add_f32_dpp v2, v2, v2 quad_perm:[2,3,0,1] row_mask:0xf bank_mask:0xf bound_ctrl:1
	s_nop 1
	v_add_f32_dpp v2, v2, v2 row_half_mirror row_mask:0xf bank_mask:0xf bound_ctrl:1
	s_nop 1
	v_add_f32_dpp v2, v2, v2 row_mirror row_mask:0xf bank_mask:0xf bound_ctrl:1
	ds_bpermute_b32 v32, v14, v2
	s_waitcnt lgkmcnt(0)
	v_add_f32_e32 v2, v2, v32
	ds_bpermute_b32 v32, v15, v2
	s_waitcnt lgkmcnt(0)
	v_add_f32_e32 v2, v2, v32
	v_fmamk_f32 v2, v2, 0x3a800000, v1
	v_mul_f32_e32 v32, 0x4f800000, v2
	v_cmp_gt_f32_e32 vcc, s29, v2
	s_nop 1
	v_cndmask_b32_e32 v2, v2, v32, vcc
	v_sqrt_f32_e32 v32, v2
	s_nop 0
	v_add_u32_e32 v33, -1, v32
	v_add_u32_e32 v34, 1, v32
	v_fma_f32 v35, -v33, v32, v2
	v_fma_f32 v37, -v34, v32, v2
	v_cmp_ge_f32_e64 s[38:39], 0, v35
	s_nop 1
	v_cndmask_b32_e64 v32, v32, v33, s[38:39]
	v_cmp_lt_f32_e64 s[38:39], 0, v37
	s_nop 1
	v_cndmask_b32_e64 v32, v32, v34, s[38:39]
	v_mul_f32_e32 v33, 0x37800000, v32
	v_cndmask_b32_e32 v32, v32, v33, vcc
	v_cmp_class_f32_e32 vcc, v2, v248
	s_nop 1
	v_cndmask_b32_e32 v2, v32, v2, vcc
	v_div_scale_f32 v32, s[4:5], v2, v2, 1.0
	v_rcp_f32_e32 v34, v32
	v_div_scale_f32 v33, vcc, 1.0, v2, 1.0
	v_fma_f32 v35, -v32, v34, 1.0
	v_fmac_f32_e32 v34, v35, v34
	v_mul_f32_e32 v35, v33, v34
	v_fma_f32 v37, -v32, v35, v33
	v_fmac_f32_e32 v35, v37, v34
	v_fma_f32 v32, -v32, v35, v33
	v_div_fmas_f32 v32, v32, v34, v35
	v_div_fixup_f32 v2, v32, v2, 1.0
	v_mul_f32_e32 v16, v16, v2
	v_mul_f32_e32 v18, v18, v2
	v_mul_f32_e32 v17, v17, v2
	v_mul_f32_e32 v19, v19, v2
	s_waitcnt vmcnt(0)
	v_mul_f32_e32 v16, v28, v16
	v_mul_f32_e32 v18, v30, v18
	v_mul_f32_e32 v17, v29, v17
	v_mul_f32_e32 v19, v31, v19
	v_bfe_u32 v28, v16, 16, 1
	v_bfe_u32 v30, v18, 16, 1
	v_bfe_u32 v29, v17, 16, 1
	v_bfe_u32 v31, v19, 16, 1
	v_add3_u32 v16, v16, v28, s1
	v_add3_u32 v18, v18, v30, s1
	v_add3_u32 v17, v17, v29, s1
	v_add3_u32 v19, v19, v31, s1
	v_lshrrev_b32_e32 v16, 16, v16
	v_lshrrev_b32_e32 v18, 16, v18
	v_and_or_b32 v16, v17, s0, v16
	v_and_or_b32 v17, v19, s0, v18
	global_store_dwordx2 v[12:13], v[16:17], off offset:-1024
	global_load_dwordx4 v[16:19], v[8:9], off offset:1024 nt
	v_mul_f32_e32 v20, v20, v2
	v_mul_f32_e32 v22, v22, v2
	v_mul_f32_e32 v21, v21, v2
	v_mul_f32_e32 v23, v23, v2
	v_mul_f32_e32 v4, v4, v2
	v_mul_f32_e32 v6, v6, v2
	v_mul_f32_e32 v5, v5, v2
	s_waitcnt vmcnt(0)
	v_mul_f32_e32 v16, v16, v20
	v_mul_f32_e32 v18, v18, v22
	v_mul_f32_e32 v17, v17, v21
	v_mul_f32_e32 v19, v19, v23
	v_bfe_u32 v20, v16, 16, 1
	v_bfe_u32 v22, v18, 16, 1
	v_bfe_u32 v21, v17, 16, 1
	v_bfe_u32 v23, v19, 16, 1
	v_add3_u32 v16, v16, v20, s1
	v_add3_u32 v18, v18, v22, s1
	v_add3_u32 v17, v17, v21, s1
	v_add3_u32 v19, v19, v23, s1
	v_lshrrev_b32_e32 v16, 16, v16
	v_lshrrev_b32_e32 v18, 16, v18
	v_and_or_b32 v16, v17, s0, v16
	v_and_or_b32 v17, v19, s0, v18
	global_store_dwordx2 v[12:13], v[16:17], off offset:-512
	global_load_dwordx4 v[16:19], v[8:9], off offset:2048 nt
	v_mul_f32_e32 v20, v24, v2
	v_mul_f32_e32 v22, v26, v2
	v_mul_f32_e32 v21, v25, v2
	v_mul_f32_e32 v23, v27, v2
	v_mul_f32_e32 v2, v7, v2
	s_waitcnt vmcnt(0)
	v_mul_f32_e32 v16, v16, v20
	v_mul_f32_e32 v18, v18, v22
	v_mul_f32_e32 v17, v17, v21
	v_mul_f32_e32 v19, v19, v23
	v_bfe_u32 v20, v16, 16, 1
	v_bfe_u32 v22, v18, 16, 1
	v_bfe_u32 v21, v17, 16, 1
	v_bfe_u32 v23, v19, 16, 1
	v_add3_u32 v16, v16, v20, s1
	v_add3_u32 v18, v18, v22, s1
	v_add3_u32 v17, v17, v21, s1
	v_add3_u32 v19, v19, v23, s1
	v_lshrrev_b32_e32 v16, 16, v16
	v_lshrrev_b32_e32 v18, 16, v18
	v_and_or_b32 v16, v17, s0, v16
	v_and_or_b32 v17, v19, s0, v18
	global_store_dwordx2 v[12:13], v[16:17], off
	global_load_dwordx4 v[16:19], v[8:9], off offset:3072 nt
	s_waitcnt vmcnt(0)
	v_mul_f32_e32 v4, v4, v16
	v_mul_f32_e32 v6, v6, v18
	v_mul_f32_e32 v5, v5, v17
	v_mul_f32_e32 v2, v2, v19
	v_bfe_u32 v7, v4, 16, 1
	v_bfe_u32 v17, v6, 16, 1
	v_bfe_u32 v16, v5, 16, 1
	v_bfe_u32 v18, v2, 16, 1
	v_add3_u32 v4, v4, v7, s1
	v_add3_u32 v6, v6, v17, s1
	v_add3_u32 v5, v5, v16, s1
	v_add3_u32 v2, v2, v18, s1
	v_lshrrev_b32_e32 v4, 16, v4
	v_lshrrev_b32_e32 v6, 16, v6
	v_and_or_b32 v4, v5, s0, v4
	v_and_or_b32 v5, v2, s0, v6
	global_store_dwordx2 v[12:13], v[4:5], off offset:512
	v_lshl_add_u64 v[12:13], v[12:13], 0, s[16:17]
	s_cbranch_scc0 .LBB0_142

.LBB0_1534:
	s_add_u32 s0, s8, s2
	s_addc_u32 s1, s9, s3
	s_add_u32 s10, s0, 0x1f800000
	s_addc_u32 s11, s1, 0
	v_lshl_add_u64 v[30:31], v[4:5], 0, s[2:3]
	global_load_dwordx4 v[10:13], v[2:3], off nt
	global_load_dwordx4 v[14:17], v0, s[0:1]
	global_load_dwordx4 v[18:21], v1, s[10:11] offset:48
	global_load_dwordx4 v[22:25], v1, s[10:11] offset:32
	global_load_dwordx4 v[26:29], v1, s[10:11] offset:16
	global_load_dwordx2 v[32:33], v[30:31], off offset:-1024
	s_add_i32 s4, s4, s90
	s_add_u32 s8, s8, s6
	s_addc_u32 s9, s9, s7
	v_lshl_add_u64 v[4:5], v[4:5], 0, s[14:15]
	s_cmp_lt_i32 s4, 0x8000
	s_waitcnt vmcnt(0)
	v_add_f32_e32 v22, v22, v23
	v_add_f32_e32 v24, v24, v25
	v_lshlrev_b32_e32 v34, 16, v32
	v_and_b32_e32 v35, 0xffff0000, v32
	v_lshlrev_b32_e32 v36, 16, v33
	v_and_b32_e32 v37, 0xffff0000, v33
	v_mov_b32_e32 v32, v15
	v_mov_b32_e32 v33, v16
	v_mov_b32_e32 v15, v17
	v_mov_b32_e32 v16, v27
	v_mov_b32_e32 v17, v28
	v_mov_b32_e32 v27, v29
	v_pk_add_f32 v[14:15], v[32:33], v[14:15]
	v_pk_add_f32 v[16:17], v[16:17], v[26:27]
	v_pk_add_f32 v[14:15], v[14:15], v[14:15] op_sel:[0,1] op_sel_hi:[1,0]
	v_pk_add_f32 v[16:17], v[16:17], v[16:17] op_sel:[0,1] op_sel_hi:[1,0]
	v_mov_b32_e32 v23, v20
	v_mov_b32_e32 v25, v21
	v_mov_b32_e32 v15, v18
	v_mov_b32_e32 v17, v19
	v_pk_add_f32 v[20:21], v[22:23], v[24:25]
	v_pk_add_f32 v[14:15], v[14:15], v[16:17]
	s_nop 0
	v_pk_add_f32 v[14:15], v[14:15], v[20:21]
	s_nop 0
	v_add_f32_e32 v14, v14, v15
	v_fmamk_f32 v14, v14, 0x3a800000, v8
	v_mul_f32_e32 v15, 0x4f800000, v14
	v_cmp_gt_f32_e32 vcc, s5, v14
	s_nop 1
	v_cndmask_b32_e32 v14, v14, v15, vcc
	v_sqrt_f32_e32 v15, v14
	s_nop 0
	v_add_u32_e32 v16, -1, v15
	v_add_u32_e32 v17, 1, v15
	v_fma_f32 v18, -v16, v15, v14
	v_fma_f32 v19, -v17, v15, v14
	v_cmp_ge_f32_e64 s[0:1], 0, v18
	s_nop 1
	v_cndmask_b32_e64 v15, v15, v16, s[0:1]
	v_cmp_lt_f32_e64 s[0:1], 0, v19
	s_nop 1
	v_cndmask_b32_e64 v15, v15, v17, s[0:1]
	v_mul_f32_e32 v16, 0x37800000, v15
	v_cndmask_b32_e32 v15, v15, v16, vcc
	v_cmp_class_f32_e32 vcc, v14, v9
	s_nop 1
	v_cndmask_b32_e32 v14, v15, v14, vcc
	v_div_scale_f32 v15, s[0:1], v14, v14, 1.0
	v_rcp_f32_e32 v17, v15
	v_div_scale_f32 v16, vcc, 1.0, v14, 1.0
	v_fma_f32 v18, -v15, v17, 1.0
	v_fmac_f32_e32 v17, v18, v17
	v_mul_f32_e32 v18, v16, v17
	v_fma_f32 v19, -v15, v18, v16
	v_fmac_f32_e32 v18, v19, v17
	v_fma_f32 v15, -v15, v18, v16
	v_div_fmas_f32 v15, v15, v17, v18
	v_div_fixup_f32 v16, v15, v14, 1.0
	v_mul_f32_e32 v14, v16, v34
	v_mul_f32_e32 v15, v16, v35
	v_mul_f32_e32 v17, v16, v36
	v_mul_f32_e32 v18, v16, v37
	v_mul_f32_e32 v10, v10, v14
	v_mul_f32_e32 v11, v11, v15
	v_mul_f32_e32 v12, v12, v17
	v_mul_f32_e32 v13, v13, v18
	global_store_dwordx4 v[6:7], v[10:13], off offset:-2048 nt
	global_load_dwordx2 v[14:15], v[30:31], off offset:-512
	s_nop 0
	global_load_dwordx4 v[10:13], v[2:3], off offset:1024 nt
	s_waitcnt vmcnt(1)
	v_lshlrev_b32_e32 v17, 16, v14
	v_and_b32_e32 v14, 0xffff0000, v14
	v_lshlrev_b32_e32 v18, 16, v15
	v_and_b32_e32 v15, 0xffff0000, v15
	v_mul_f32_e32 v17, v16, v17
	v_mul_f32_e32 v14, v16, v14
	v_mul_f32_e32 v18, v16, v18
	v_mul_f32_e32 v15, v16, v15
	s_waitcnt vmcnt(0)
	v_mul_f32_e32 v10, v10, v17
	v_mul_f32_e32 v11, v11, v14
	v_mul_f32_e32 v12, v12, v18
	v_mul_f32_e32 v13, v13, v15
	global_store_dwordx4 v[6:7], v[10:13], off offset:-1024 nt
	global_load_dwordx2 v[14:15], v[30:31], off
	s_nop 0
	global_load_dwordx4 v[10:13], v[2:3], off offset:2048 nt
	s_waitcnt vmcnt(1)
	v_lshlrev_b32_e32 v17, 16, v14
	v_and_b32_e32 v14, 0xffff0000, v14
	v_lshlrev_b32_e32 v18, 16, v15
	v_and_b32_e32 v15, 0xffff0000, v15
	v_mul_f32_e32 v17, v16, v17
	v_mul_f32_e32 v14, v16, v14
	v_mul_f32_e32 v18, v16, v18
	v_mul_f32_e32 v15, v16, v15
	s_waitcnt vmcnt(0)
	v_mul_f32_e32 v10, v10, v17
	v_mul_f32_e32 v11, v11, v14
	v_mul_f32_e32 v12, v12, v18
	v_mul_f32_e32 v13, v13, v15
	global_store_dwordx4 v[6:7], v[10:13], off nt
	global_load_dwordx2 v[14:15], v[30:31], off offset:512
	s_nop 0
	global_load_dwordx4 v[10:13], v[2:3], off offset:3072 nt
	s_waitcnt vmcnt(1)
	v_lshlrev_b32_e32 v17, 16, v14
	v_and_b32_e32 v14, 0xffff0000, v14
	v_lshlrev_b32_e32 v18, 16, v15
	v_and_b32_e32 v15, 0xffff0000, v15
	v_mul_f32_e32 v17, v16, v17
	v_mul_f32_e32 v14, v16, v14
	v_mul_f32_e32 v18, v16, v18
	v_mul_f32_e32 v15, v16, v15
	s_waitcnt vmcnt(0)
	v_mul_f32_e32 v10, v10, v17
	v_mul_f32_e32 v11, v11, v14
	v_mul_f32_e32 v12, v12, v18
	v_mul_f32_e32 v13, v13, v15
	global_store_dwordx4 v[6:7], v[10:13], off offset:1024 nt
	v_lshl_add_u64 v[6:7], v[6:7], 0, s[12:13]
	s_cbranch_scc1 .LBB0_1534
